# MLA softmax: exponent arguments via v_pk_fma_f32 on accumulator pairs and row sum via v_pk_add_f32 tree (31 fewer VALU per key tile), on top of SB K-prefetch
# speedup vs baseline: 1.0073x; 1.0073x over previous
.LBB0_465:
	s_mov_b32 s100, 0x3dd53b94
	v_mul_f32_e32 v208, 0xbdd53b94, v206
	s_nop 0
	v_pk_fma_f32 v[82:83], v[82:83], s[100:101], v[208:209] op_sel_hi:[1,0,0]
	v_pk_fma_f32 v[66:67], v[66:67], s[100:101], v[208:209] op_sel_hi:[1,0,0]
	v_exp_f32_e32 v82, v82
	v_exp_f32_e32 v83, v83
	v_pk_fma_f32 v[84:85], v[84:85], s[100:101], v[208:209] op_sel_hi:[1,0,0]
	v_exp_f32_e32 v210, v66
	v_exp_f32_e32 v211, v67
	v_pk_fma_f32 v[68:69], v[68:69], s[100:101], v[208:209] op_sel_hi:[1,0,0]
	v_exp_f32_e32 v84, v84
	v_exp_f32_e32 v85, v85
	v_pk_fma_f32 v[86:87], v[86:87], s[100:101], v[208:209] op_sel_hi:[1,0,0]
	v_pk_add_f32 v[66:67], v[82:83], v[210:211]
	v_exp_f32_e32 v212, v68
	v_exp_f32_e32 v213, v69
	v_pk_fma_f32 v[70:71], v[70:71], s[100:101], v[208:209] op_sel_hi:[1,0,0]
	v_exp_f32_e32 v86, v86
	v_exp_f32_e32 v87, v87
	v_pk_fma_f32 v[88:89], v[88:89], s[100:101], v[208:209] op_sel_hi:[1,0,0]
	v_pk_add_f32 v[68:69], v[84:85], v[212:213]
	v_exp_f32_e32 v214, v70
	v_exp_f32_e32 v215, v71
	v_pk_fma_f32 v[72:73], v[72:73], s[100:101], v[208:209] op_sel_hi:[1,0,0]
	v_exp_f32_e32 v88, v88
	v_exp_f32_e32 v89, v89
	v_pk_fma_f32 v[90:91], v[90:91], s[100:101], v[208:209] op_sel_hi:[1,0,0]
	v_pk_add_f32 v[70:71], v[86:87], v[214:215]
	v_exp_f32_e32 v216, v72
	v_exp_f32_e32 v217, v73
	v_pk_fma_f32 v[74:75], v[74:75], s[100:101], v[208:209] op_sel_hi:[1,0,0]
	v_exp_f32_e32 v90, v90
	v_exp_f32_e32 v91, v91
	v_pk_fma_f32 v[92:93], v[92:93], s[100:101], v[208:209] op_sel_hi:[1,0,0]
	v_pk_add_f32 v[72:73], v[88:89], v[216:217]
	v_exp_f32_e32 v218, v74
	v_exp_f32_e32 v219, v75
	v_pk_fma_f32 v[76:77], v[76:77], s[100:101], v[208:209] op_sel_hi:[1,0,0]
	v_exp_f32_e32 v92, v92
	v_exp_f32_e32 v93, v93
	v_pk_fma_f32 v[94:95], v[94:95], s[100:101], v[208:209] op_sel_hi:[1,0,0]
	v_pk_add_f32 v[74:75], v[90:91], v[218:219]
	v_exp_f32_e32 v220, v76
	v_exp_f32_e32 v221, v77
	v_pk_fma_f32 v[78:79], v[78:79], s[100:101], v[208:209] op_sel_hi:[1,0,0]
	v_exp_f32_e32 v94, v94
	v_exp_f32_e32 v95, v95
	v_pk_fma_f32 v[96:97], v[96:97], s[100:101], v[208:209] op_sel_hi:[1,0,0]
	v_pk_add_f32 v[76:77], v[92:93], v[220:221]
	v_exp_f32_e32 v222, v78
	v_exp_f32_e32 v223, v79
	v_pk_fma_f32 v[80:81], v[80:81], s[100:101], v[208:209] op_sel_hi:[1,0,0]
	v_exp_f32_e32 v96, v96
	v_exp_f32_e32 v97, v97
	v_pk_add_f32 v[78:79], v[94:95], v[222:223]
	v_exp_f32_e32 v208, v80
	v_exp_f32_e32 v209, v81
	s_nop 0
	v_pk_add_f32 v[80:81], v[96:97], v[208:209]
	v_pk_add_f32 v[66:67], v[66:67], v[68:69]
	v_pk_add_f32 v[70:71], v[70:71], v[72:73]
	v_pk_add_f32 v[74:75], v[74:75], v[76:77]
	v_pk_add_f32 v[78:79], v[78:79], v[80:81]
	v_pk_add_f32 v[66:67], v[66:67], v[70:71]
	v_pk_add_f32 v[74:75], v[74:75], v[78:79]
	v_pk_add_f32 v[66:67], v[66:67], v[74:75]
	v_cvt_pk_bf16_f32 v73, v96, v97
	s_mul_i32 s48, s47, 0x5000
	v_add_f32_e32 v97, v66, v67
	v_cvt_pk_bf16_f32 v66, v82, v83
	v_cvt_pk_bf16_f32 v67, v84, v85
	v_cvt_pk_bf16_f32 v68, v86, v87
	v_cvt_pk_bf16_f32 v69, v88, v89
	v_cvt_pk_bf16_f32 v70, v90, v91
	v_cvt_pk_bf16_f32 v71, v92, v93
	v_cvt_pk_bf16_f32 v72, v94, v95
	v_add_u32_e32 v90, s48, v204
	ds_read_b128 v[82:85], v90 offset:53248
	ds_read_b128 v[86:89], v90 offset:58368
	v_cvt_pk_bf16_f32 v74, v210, v211
	v_cvt_pk_bf16_f32 v75, v212, v213
	v_cvt_pk_bf16_f32 v76, v214, v215
	v_cvt_pk_bf16_f32 v77, v216, v217
	v_cvt_pk_bf16_f32 v78, v218, v219
	v_cvt_pk_bf16_f32 v79, v220, v221
	v_cvt_pk_bf16_f32 v80, v222, v223
	v_cvt_pk_bf16_f32 v81, v208, v209
	v_add_u32_e32 v91, 0xd000, v90
	s_waitcnt lgkmcnt(1)
	v_mfma_f32_32x32x16_bf16 v[50:65], v[82:85], v[66:69], v[50:65]
	ds_read_b128 v[82:85], v90 offset:63488
	s_waitcnt lgkmcnt(1)
	v_mfma_f32_32x32x16_bf16 v[34:49], v[86:89], v[66:69], v[34:49]
	ds_read_b128 v[86:89], v91 offset:15360
	s_waitcnt lgkmcnt(1)
	v_mfma_f32_32x32x16_bf16 v[18:33], v[82:85], v[66:69], v[18:33]
	ds_read_b128 v[82:85], v90 offset:53264
	s_waitcnt lgkmcnt(1)
	v_mfma_f32_32x32x16_bf16 v[2:17], v[86:89], v[66:69], v[2:17]
	ds_read_b128 v[66:69], v90 offset:58384
	s_waitcnt lgkmcnt(1)
	v_mfma_f32_32x32x16_bf16 v[50:65], v[82:85], v[70:73], v[50:65]
	ds_read_b128 v[82:85], v90 offset:63504
	s_waitcnt lgkmcnt(1)
	v_mfma_f32_32x32x16_bf16 v[34:49], v[66:69], v[70:73], v[34:49]
	ds_read_b128 v[66:69], v91 offset:15376
	s_waitcnt lgkmcnt(1)
	v_mfma_f32_32x32x16_bf16 v[18:33], v[82:85], v[70:73], v[18:33]
	ds_read_b128 v[82:85], v90 offset:53312
	s_waitcnt lgkmcnt(1)
	v_mfma_f32_32x32x16_bf16 v[2:17], v[66:69], v[70:73], v[2:17]
	ds_read_b128 v[66:69], v90 offset:58432
	s_waitcnt lgkmcnt(1)
	v_mfma_f32_32x32x16_bf16 v[50:65], v[82:85], v[74:77], v[50:65]
	ds_read_b128 v[70:73], v90 offset:63552
	s_waitcnt lgkmcnt(1)
	v_mfma_f32_32x32x16_bf16 v[34:49], v[66:69], v[74:77], v[34:49]
	ds_read_b128 v[66:69], v91 offset:15424
	s_waitcnt lgkmcnt(1)
	v_mfma_f32_32x32x16_bf16 v[18:33], v[70:73], v[74:77], v[18:33]
	ds_read_b128 v[70:73], v90 offset:53328
	s_waitcnt lgkmcnt(1)
	v_mfma_f32_32x32x16_bf16 v[2:17], v[66:69], v[74:77], v[2:17]
	ds_read_b128 v[66:69], v90 offset:58448
	s_waitcnt lgkmcnt(1)
	v_mfma_f32_32x32x16_bf16 v[50:65], v[70:73], v[78:81], v[50:65]
	ds_read_b128 v[70:73], v90 offset:63568
	s_waitcnt lgkmcnt(1)
	v_mfma_f32_32x32x16_bf16 v[34:49], v[66:69], v[78:81], v[34:49]
	ds_read_b128 v[66:69], v91 offset:15440
	s_waitcnt lgkmcnt(1)
	v_mfma_f32_32x32x16_bf16 v[18:33], v[70:73], v[78:81], v[18:33]
	s_waitcnt lgkmcnt(0)
	v_mfma_f32_32x32x16_bf16 v[2:17], v[66:69], v[78:81], v[2:17]
	v_add_f32_e32 v205, v97, v205
	s_andn2_b64 vcc, exec, s[26:27]
	s_cbranch_vccz .LBB0_467
	s_branch .LBB0_468

.LBB0_478:
	s_mov_b32 s100, 0x3dd53b94
	v_mul_f32_e32 v208, 0xbdd53b94, v207
	s_nop 0
	v_pk_fma_f32 v[82:83], v[82:83], s[100:101], v[208:209] op_sel_hi:[1,0,0]
	v_pk_fma_f32 v[66:67], v[66:67], s[100:101], v[208:209] op_sel_hi:[1,0,0]
	v_exp_f32_e32 v82, v82
	v_exp_f32_e32 v83, v83
	v_pk_fma_f32 v[84:85], v[84:85], s[100:101], v[208:209] op_sel_hi:[1,0,0]
	v_exp_f32_e32 v210, v66
	v_exp_f32_e32 v211, v67
	v_pk_fma_f32 v[68:69], v[68:69], s[100:101], v[208:209] op_sel_hi:[1,0,0]
	v_exp_f32_e32 v84, v84
	v_exp_f32_e32 v85, v85
	v_pk_fma_f32 v[86:87], v[86:87], s[100:101], v[208:209] op_sel_hi:[1,0,0]
	v_pk_add_f32 v[66:67], v[82:83], v[210:211]
	v_exp_f32_e32 v212, v68
	v_exp_f32_e32 v213, v69
	v_pk_fma_f32 v[70:71], v[70:71], s[100:101], v[208:209] op_sel_hi:[1,0,0]
	v_exp_f32_e32 v86, v86
	v_exp_f32_e32 v87, v87
	v_pk_fma_f32 v[88:89], v[88:89], s[100:101], v[208:209] op_sel_hi:[1,0,0]
	v_pk_add_f32 v[68:69], v[84:85], v[212:213]
	v_exp_f32_e32 v214, v70
	v_exp_f32_e32 v215, v71
	v_pk_fma_f32 v[72:73], v[72:73], s[100:101], v[208:209] op_sel_hi:[1,0,0]
	v_exp_f32_e32 v88, v88
	v_exp_f32_e32 v89, v89
	v_pk_fma_f32 v[90:91], v[90:91], s[100:101], v[208:209] op_sel_hi:[1,0,0]
	v_pk_add_f32 v[70:71], v[86:87], v[214:215]
	v_exp_f32_e32 v216, v72
	v_exp_f32_e32 v217, v73
	v_pk_fma_f32 v[74:75], v[74:75], s[100:101], v[208:209] op_sel_hi:[1,0,0]
	v_exp_f32_e32 v90, v90
	v_exp_f32_e32 v91, v91
	v_pk_fma_f32 v[92:93], v[92:93], s[100:101], v[208:209] op_sel_hi:[1,0,0]
	v_pk_add_f32 v[72:73], v[88:89], v[216:217]
	v_exp_f32_e32 v218, v74
	v_exp_f32_e32 v219, v75
	v_pk_fma_f32 v[76:77], v[76:77], s[100:101], v[208:209] op_sel_hi:[1,0,0]
	v_exp_f32_e32 v92, v92
	v_exp_f32_e32 v93, v93
	v_pk_fma_f32 v[94:95], v[94:95], s[100:101], v[208:209] op_sel_hi:[1,0,0]
	v_pk_add_f32 v[74:75], v[90:91], v[218:219]
	v_exp_f32_e32 v220, v76
	v_exp_f32_e32 v221, v77
	v_pk_fma_f32 v[78:79], v[78:79], s[100:101], v[208:209] op_sel_hi:[1,0,0]
	v_exp_f32_e32 v94, v94
	v_exp_f32_e32 v95, v95
	v_pk_fma_f32 v[96:97], v[96:97], s[100:101], v[208:209] op_sel_hi:[1,0,0]
	v_pk_add_f32 v[76:77], v[92:93], v[220:221]
	v_exp_f32_e32 v222, v78
	v_exp_f32_e32 v223, v79
	v_pk_fma_f32 v[80:81], v[80:81], s[100:101], v[208:209] op_sel_hi:[1,0,0]
	v_exp_f32_e32 v96, v96
	v_exp_f32_e32 v97, v97
	v_pk_add_f32 v[78:79], v[94:95], v[222:223]
	v_exp_f32_e32 v208, v80
	v_exp_f32_e32 v209, v81
	s_nop 0
	v_pk_add_f32 v[80:81], v[96:97], v[208:209]
	v_pk_add_f32 v[66:67], v[66:67], v[68:69]
	v_pk_add_f32 v[70:71], v[70:71], v[72:73]
	v_pk_add_f32 v[74:75], v[74:75], v[76:77]
	v_pk_add_f32 v[78:79], v[78:79], v[80:81]
	v_pk_add_f32 v[66:67], v[66:67], v[70:71]
	v_pk_add_f32 v[74:75], v[74:75], v[78:79]
	v_pk_add_f32 v[66:67], v[66:67], v[74:75]
	v_cvt_pk_bf16_f32 v73, v96, v97
	s_mul_i32 s22, s17, 0x5000
	v_add_f32_e32 v97, v66, v67
	v_cvt_pk_bf16_f32 v66, v82, v83
	v_cvt_pk_bf16_f32 v67, v84, v85
	v_cvt_pk_bf16_f32 v68, v86, v87
	v_cvt_pk_bf16_f32 v69, v88, v89
	v_cvt_pk_bf16_f32 v70, v90, v91
	v_cvt_pk_bf16_f32 v71, v92, v93
	v_cvt_pk_bf16_f32 v72, v94, v95
	v_add_u32_e32 v90, s22, v206
	ds_read_b128 v[82:85], v90 offset:53248
	ds_read_b128 v[86:89], v90 offset:58368
	v_cvt_pk_bf16_f32 v74, v210, v211
	v_cvt_pk_bf16_f32 v75, v212, v213
	v_cvt_pk_bf16_f32 v76, v214, v215
	v_cvt_pk_bf16_f32 v77, v216, v217
	v_cvt_pk_bf16_f32 v78, v218, v219
	v_cvt_pk_bf16_f32 v79, v220, v221
	v_cvt_pk_bf16_f32 v80, v222, v223
	v_cvt_pk_bf16_f32 v81, v208, v209
	v_add_u32_e32 v91, 0xd000, v90
	s_waitcnt lgkmcnt(1)
	v_mfma_f32_32x32x16_bf16 v[50:65], v[82:85], v[66:69], v[50:65]
	ds_read_b128 v[82:85], v90 offset:63488
	s_waitcnt lgkmcnt(1)
	v_mfma_f32_32x32x16_bf16 v[34:49], v[86:89], v[66:69], v[34:49]
	ds_read_b128 v[86:89], v91 offset:15360
	s_waitcnt lgkmcnt(1)
	v_mfma_f32_32x32x16_bf16 v[18:33], v[82:85], v[66:69], v[18:33]
	ds_read_b128 v[82:85], v90 offset:53264
	s_waitcnt lgkmcnt(1)
	v_mfma_f32_32x32x16_bf16 v[2:17], v[86:89], v[66:69], v[2:17]
	ds_read_b128 v[66:69], v90 offset:58384
	s_waitcnt lgkmcnt(1)
	v_mfma_f32_32x32x16_bf16 v[50:65], v[82:85], v[70:73], v[50:65]
	ds_read_b128 v[82:85], v90 offset:63504
	s_waitcnt lgkmcnt(1)
	v_mfma_f32_32x32x16_bf16 v[34:49], v[66:69], v[70:73], v[34:49]
	ds_read_b128 v[66:69], v91 offset:15376
	s_waitcnt lgkmcnt(1)
	v_mfma_f32_32x32x16_bf16 v[18:33], v[82:85], v[70:73], v[18:33]
	ds_read_b128 v[82:85], v90 offset:53312
	s_waitcnt lgkmcnt(1)
	v_mfma_f32_32x32x16_bf16 v[2:17], v[66:69], v[70:73], v[2:17]
	ds_read_b128 v[66:69], v90 offset:58432
	s_waitcnt lgkmcnt(1)
	v_mfma_f32_32x32x16_bf16 v[50:65], v[82:85], v[74:77], v[50:65]
	ds_read_b128 v[70:73], v90 offset:63552
	s_waitcnt lgkmcnt(1)
	v_mfma_f32_32x32x16_bf16 v[34:49], v[66:69], v[74:77], v[34:49]
	ds_read_b128 v[66:69], v91 offset:15424
	s_waitcnt lgkmcnt(1)
	v_mfma_f32_32x32x16_bf16 v[18:33], v[70:73], v[74:77], v[18:33]
	ds_read_b128 v[70:73], v90 offset:53328
	s_waitcnt lgkmcnt(1)
	v_mfma_f32_32x32x16_bf16 v[2:17], v[66:69], v[74:77], v[2:17]
	ds_read_b128 v[66:69], v90 offset:58448
	s_waitcnt lgkmcnt(1)
	v_mfma_f32_32x32x16_bf16 v[50:65], v[70:73], v[78:81], v[50:65]
	ds_read_b128 v[70:73], v90 offset:63568
	s_waitcnt lgkmcnt(1)
	v_mfma_f32_32x32x16_bf16 v[34:49], v[66:69], v[78:81], v[34:49]
	ds_read_b128 v[66:69], v91 offset:15440
	s_waitcnt lgkmcnt(1)
	v_mfma_f32_32x32x16_bf16 v[18:33], v[70:73], v[78:81], v[18:33]
	s_waitcnt lgkmcnt(0)
	v_mfma_f32_32x32x16_bf16 v[2:17], v[66:69], v[78:81], v[2:17]
	v_add_f32_e32 v205, v97, v205
	s_andn2_b64 vcc, exec, s[12:13]
	s_cbranch_vccz .LBB0_480
	s_branch .LBB0_481
